# W2 weight conversion: workgroups with blockIdx bit3 set run their share before G4 instead of after it (half the chip streams while the other half computes)
# baseline (speedup 1.0000x reference)
; #define IN(k) (lo <= (k) && (k) < hi && ((F = make_frame((LAS unsigned char*)lds_raw, wv)), true))
; #define SEAM(k) do { if ((k) + 1 < hi) xcd_barrier(bar, tid_now(wv) == 0); } while (0)
; DI void phase_expert_weights(const Frame& F, int l, int which) {
;     ...
;     else {
;         constexpr int IPM = (FF / 64) * (D / 32);
;         for (int it = F.gw; it < NE * IPM; it += F.NGW) { const int mtx = l * NE + it / IPM, r = it % IPM;
;             transpose_item(F.ap->in[34] + (size_t)mtx * FF * D, FF, D, (bf16_t*)(ws + WS_W2 + (size_t)mtx * D * FF), 2, scr, r, F.lane); }
; __global__ void __launch_bounds__(NTHR, 2) fwd_kernel(Args args) {
;     ...
;         if (IN(pb + 10)) { phase_expert_weights(F, l, 1); SEAM(pb + 10); }
.LBB0_1160:
	s_cmp_gt_i32 s96, s10
	s_cselect_b64 s[4:5], -1, 0
	s_cmp_ge_i32 s10, s97
	v_readlane_b32 s2, v253, 58
	s_cselect_b64 s[6:7], -1, 0
	s_or_b32 s24, s2, 13
	s_cmp_lt_i32 s24, s97
	s_cselect_b64 s[30:31], -1, 0
	s_or_b64 s[4:5], s[4:5], s[6:7]
	s_and_b64 vcc, exec, s[4:5]
	s_cbranch_vccnz .LBB0_1301
	s_bitcmp0_b32 s94, 3
	s_cbranch_scc1 .Lpre2_skip
	s_mov_b32 s22, s10
	s_mov_b32 s23, s39
	s_mov_b64 s[36:37], s[42:43]
	v_mov_b32_e32 v149, v1
	v_mov_b32_e32 v150, v2
	v_mov_b32_e32 v151, v3
	v_mov_b32_e32 v152, v5
	v_mov_b32_e32 v153, v6
	v_mov_b32_e32 v154, v7
	v_mov_b32_e32 v155, v8
	v_mov_b32_e32 v156, v9
	v_mov_b32_e32 v157, v10
	v_mov_b32_e32 v158, v11
	v_mov_b32_e32 v159, v12
	v_mov_b32_e32 v160, v13
	v_mov_b32_e32 v161, v14
	v_mov_b32_e32 v162, v15
	v_mov_b32_e32 v163, v16
	v_mov_b32_e32 v164, v17
	v_mov_b32_e32 v165, v25
	v_mov_b32_e32 v166, v26
	v_mov_b32_e32 v167, v27
	v_mov_b32_e32 v168, v30
	v_mov_b32_e32 v169, v31
	v_mov_b32_e32 v170, v32
	v_mov_b32_e32 v171, v192
	s_mov_b64 s[4:5], s[58:59]
	v_readlane_b32 s2, v252, 0
	v_mbcnt_lo_u32_b32 v0, -1, 0
	v_mbcnt_hi_u32_b32 v0, -1, v0
	s_mov_b32 s6, s94
	s_nop 0
	v_add_u32_e32 v1, s2, v0
	s_mov_b32 s2, s60
	s_and_b32 s7, s2, 7
	s_cmp_lg_u32 s7, 0
	v_readfirstlane_b32 s7, v1
	s_cbranch_scc1 .Lpre2_1248
	s_ashr_i32 s9, s6, 31
	s_lshr_b32 s9, s9, 29
	s_add_i32 s9, s6, s9
	s_ashr_i32 s10, s9, 3
	s_and_b32 s9, s9, -8
	s_ashr_i32 s8, s2, 3
	s_sub_i32 s6, s6, s9
	s_mul_i32 s6, s8, s6
	s_add_i32 s6, s6, s10

; #define LAS __attribute__((address_space(3)))
; DI void moe_tables(const Frame& F, int l) {
;     LAS int* pstart = (LAS int*)(F.lds + L_PSTART); LAS int* ntl = (LAS int*)(F.lds + L_NTILES); LAS int* tile_e = (LAS int*)(F.lds + L_TILEE);
;     __syncthreads();
;     if (F.tid < 64) { const unsigned* gc = (const unsigned*)(F.ws + WS_CTL) + CW_GCNT + l * 32; const int e = F.lane;
;         const int c = e < 32 ? (int)__hip_atomic_load(gc + e, __ATOMIC_RELAXED, __HIP_MEMORY_SCOPE_AGENT) : 0; const int tl = (c + 255) >> 8;
.Lpre2_done:
	s_mov_b32 s10, s22
	s_mov_b32 s39, s23
	s_mov_b64 s[42:43], s[36:37]
	v_mov_b32_e32 v1, v149
	v_mov_b32_e32 v2, v150
	v_mov_b32_e32 v3, v151
	v_mov_b32_e32 v5, v152
	v_mov_b32_e32 v6, v153
	v_mov_b32_e32 v7, v154
	v_mov_b32_e32 v8, v155
	v_mov_b32_e32 v9, v156
	v_mov_b32_e32 v10, v157
	v_mov_b32_e32 v11, v158
	v_mov_b32_e32 v12, v159
	v_mov_b32_e32 v13, v160
	v_mov_b32_e32 v14, v161
	v_mov_b32_e32 v15, v162
	v_mov_b32_e32 v16, v163
	v_mov_b32_e32 v17, v164
	v_mov_b32_e32 v25, v165
	v_mov_b32_e32 v26, v166
	v_mov_b32_e32 v27, v167
	v_mov_b32_e32 v30, v168
	v_mov_b32_e32 v31, v169
	v_mov_b32_e32 v32, v170
	v_mov_b32_e32 v192, v171
.Lpre2_skip:
	s_mov_b64 s[4:5], s[58:59]
	v_readlane_b32 s2, v252, 0
	s_waitcnt lgkmcnt(0)
	v_mbcnt_lo_u32_b32 v0, -1, 0
	v_mbcnt_hi_u32_b32 v0, -1, v0
	s_mov_b32 s19, s60
	v_add_u32_e32 v4, s2, v0
	s_mov_b32 s2, s94
	s_load_dwordx2 s[50:51], s[4:5], 0x128
	v_cmp_gt_i32_e32 vcc, 64, v4
	s_waitcnt vmcnt(0) lgkmcnt(0)
	s_barrier
	s_and_saveexec_b64 s[4:5], vcc
	s_cbranch_execz .LBB0_1173
	v_and_b32_e32 v0, 63, v0
	v_cmp_gt_u32_e64 s[36:37], 32, v0
	v_mov_b32_e32 v3, 0
	s_and_saveexec_b64 s[6:7], s[36:37]
	s_cbranch_execz .LBB0_1164
	s_lshl_b64 s[8:9], s[28:29], 2
	s_add_u32 s8, s50, s8
	s_addc_u32 s9, s51, s9
	v_lshlrev_b32_e32 v192, 2, v0
	v_lshl_add_u64 v[2:3], s[8:9], 0, v[192:193]
	v_add_co_u32_e32 v2, vcc, 0x10000, v2
	s_nop 1
	v_addc_co_u32_e32 v3, vcc, 0, v3, vcc
	global_load_dword v3, v[2:3], off sc1

; #define IN(k) (lo <= (k) && (k) < hi && ((F = make_frame((LAS unsigned char*)lds_raw, wv)), true))
; #define SEAM(k) do { if ((k) + 1 < hi) xcd_barrier(bar, tid_now(wv) == 0); } while (0)
; DI void phase_expert_weights(const Frame& F, int l, int which) {
;     ...
;     else {
;         constexpr int IPM = (FF / 64) * (D / 32);
;         for (int it = F.gw; it < NE * IPM; it += F.NGW) { const int mtx = l * NE + it / IPM, r = it % IPM;
;             transpose_item(F.ap->in[34] + (size_t)mtx * FF * D, FF, D, (bf16_t*)(ws + WS_W2 + (size_t)mtx * D * FF), 2, scr, r, F.lane); }
; __global__ void __launch_bounds__(NTHR, 2) fwd_kernel(Args args) {
;     ...
;         if (IN(pb + 10)) { phase_expert_weights(F, l, 1); SEAM(pb + 10); }
.LBB0_1246:
	s_bitcmp1_b32 s94, 3
	s_cbranch_scc1 .LBB0_1251
	s_mov_b64 s[4:5], s[58:59]
	v_readlane_b32 s2, v252, 0
	v_mbcnt_lo_u32_b32 v0, -1, 0
	v_mbcnt_hi_u32_b32 v0, -1, v0
	s_mov_b32 s6, s94
	s_nop 0
	v_add_u32_e32 v1, s2, v0
	s_mov_b32 s2, s60
	s_and_b32 s7, s2, 7
	s_cmp_lg_u32 s7, 0
	v_readfirstlane_b32 s7, v1
	s_cbranch_scc1 .LBB0_1248
	s_ashr_i32 s9, s6, 31
	s_lshr_b32 s9, s9, 29
	s_add_i32 s9, s6, s9
	s_ashr_i32 s10, s9, 3
	s_and_b32 s9, s9, -8
	s_ashr_i32 s8, s2, 3
	s_sub_i32 s6, s6, s9
	s_mul_i32 s6, s8, s6
	s_add_i32 s6, s6, s10
